# speedup vs baseline: 1.0039x; 1.0039x over previous
_Z11pool_kernelPKfPKiPDF16_:
	s_load_dwordx2 s[4:5], s[0:1], 0x8
	v_lshrrev_b32_e32 v12, 7, v0
	v_lshl_or_b32 v6, s2, 1, v12
	v_ashrrev_i32_e32 v7, 31, v6
	v_and_b32_e32 v10, 31, v0
	s_waitcnt lgkmcnt(0)
	v_lshl_add_u64 v[2:3], v[6:7], 2, s[4:5]
	global_load_dwordx2 v[8:9], v[2:3], off
	v_mov_b32_e32 v2, 0
	v_and_b32_e32 v1, 63, v0
	v_bfe_u32 v7, v0, 6, 1
	v_cmp_gt_u32_e32 vcc, 25, v10
	v_mov_b32_e32 v3, v2
	v_mov_b32_e32 v4, v2
	v_mov_b32_e32 v5, v2
	s_and_saveexec_b64 s[2:3], vcc
	s_cbranch_execz .LBB3_6
	v_lshrrev_b32_e32 v2, 5, v1
	v_lshl_or_b32 v2, v7, 1, v2
	s_waitcnt vmcnt(0)
	v_add_u32_e32 v13, v2, v8
	v_mov_b32_e32 v5, 0
	v_cmp_lt_i32_e32 vcc, v13, v9
	v_mov_b32_e32 v4, v5
	v_mov_b32_e32 v3, v5
	v_mov_b32_e32 v2, v5
	s_and_saveexec_b64 s[4:5], vcc
	s_cbranch_execz .LBB3_5
	s_load_dwordx2 s[6:7], s[0:1], 0x0
	v_lshlrev_b32_e32 v2, 4, v10
	v_mov_b32_e32 v3, 0
	s_movk_i32 s8, 0x190
	v_mad_i64_i32 v[4:5], s[8:9], v13, s8, v[2:3]
	s_waitcnt lgkmcnt(0)
	v_lshl_add_u64 v[4:5], s[6:7], 0, v[4:5]
	s_mov_b64 s[8:9], 0x960
	v_lshl_add_u64 v[10:11], v[4:5], 0, s[8:9]
	s_mov_b64 s[8:9], 0x1900
	v_lshl_add_u64 v[48:49], v[10:11], 0, s[8:9]
	s_mov_b64 s[6:7], 0
	s_mov_b64 s[8:9], 0x3200
	v_mov_b32_e32 v2, v3
	v_mov_b32_e32 v4, v3
	v_mov_b32_e32 v5, v3
.LBB3_3:
	v_add_u32_e32 v30, 4, v13
	v_cmp_lt_i32_e64 s[10:11], v30, v9
	v_add_u32_e32 v30, 8, v13
	v_cmp_lt_i32_e64 s[12:13], v30, v9
	v_add_u32_e32 v30, 12, v13
	v_cmp_lt_i32_e64 s[14:15], v30, v9
	v_add_u32_e32 v30, 16, v13
	v_cmp_lt_i32_e64 s[18:19], v30, v9
	v_add_u32_e32 v30, 20, v13
	v_cmp_lt_i32_e64 s[20:21], v30, v9
	v_add_u32_e32 v30, 24, v13
	v_cmp_lt_i32_e64 s[22:23], v30, v9
	v_add_u32_e32 v30, 28, v13
	v_cmp_lt_i32_e64 s[24:25], v30, v9
	s_mov_b64 s[16:17], exec
	global_load_dwordx4 v[14:17], v[10:11], off offset:-2400
	s_and_b64 exec, s[16:17], s[10:11]
	s_cbranch_execz .Lpool_ld_done
	global_load_dwordx4 v[18:21], v[10:11], off offset:-800
	s_and_b64 exec, s[16:17], s[12:13]
	s_cbranch_execz .Lpool_ld_done
	global_load_dwordx4 v[22:25], v[10:11], off offset:800
	s_and_b64 exec, s[16:17], s[14:15]
	s_cbranch_execz .Lpool_ld_done
	global_load_dwordx4 v[26:29], v[10:11], off offset:2400
	s_and_b64 exec, s[16:17], s[18:19]
	s_cbranch_execz .Lpool_ld_done
	global_load_dwordx4 v[32:35], v[48:49], off offset:-2400
	s_and_b64 exec, s[16:17], s[20:21]
	s_cbranch_execz .Lpool_ld_done
	global_load_dwordx4 v[36:39], v[48:49], off offset:-800
	s_and_b64 exec, s[16:17], s[22:23]
	s_cbranch_execz .Lpool_ld_done
	global_load_dwordx4 v[40:43], v[48:49], off offset:800
	s_and_b64 exec, s[16:17], s[24:25]
	s_cbranch_execz .Lpool_ld_done
	global_load_dwordx4 v[44:47], v[48:49], off offset:2400
.Lpool_ld_done:
	s_mov_b64 exec, s[16:17]
	v_add_u32_e32 v13, 32, v13
	v_cmp_ge_i32_e32 vcc, v13, v9
	v_lshl_add_u64 v[10:11], v[10:11], 0, s[8:9]
	v_lshl_add_u64 v[48:49], v[48:49], 0, s[8:9]
	s_or_b64 s[6:7], vcc, s[6:7]
	s_waitcnt vmcnt(0)
	v_pk_add_f32 v[2:3], v[2:3], v[14:15]
	v_pk_add_f32 v[4:5], v[4:5], v[16:17]
	s_and_b64 exec, s[16:17], s[10:11]
	v_pk_add_f32 v[2:3], v[2:3], v[18:19]
	v_pk_add_f32 v[4:5], v[4:5], v[20:21]
	s_and_b64 exec, s[16:17], s[12:13]
	v_pk_add_f32 v[2:3], v[2:3], v[22:23]
	v_pk_add_f32 v[4:5], v[4:5], v[24:25]
	s_and_b64 exec, s[16:17], s[14:15]
	v_pk_add_f32 v[2:3], v[2:3], v[26:27]
	v_pk_add_f32 v[4:5], v[4:5], v[28:29]
	s_and_b64 exec, s[16:17], s[18:19]
	v_pk_add_f32 v[2:3], v[2:3], v[32:33]
	v_pk_add_f32 v[4:5], v[4:5], v[34:35]
	s_and_b64 exec, s[16:17], s[20:21]
	v_pk_add_f32 v[2:3], v[2:3], v[36:37]
	v_pk_add_f32 v[4:5], v[4:5], v[38:39]
	s_and_b64 exec, s[16:17], s[22:23]
	v_pk_add_f32 v[2:3], v[2:3], v[40:41]
	v_pk_add_f32 v[4:5], v[4:5], v[42:43]
	s_and_b64 exec, s[16:17], s[24:25]
	v_pk_add_f32 v[2:3], v[2:3], v[44:45]
	v_pk_add_f32 v[4:5], v[4:5], v[46:47]
	s_mov_b64 exec, s[16:17]
	s_andn2_b64 exec, exec, s[6:7]
	s_cbranch_execnz .LBB3_3
	s_or_b64 exec, exec, s[6:7]

	.amdhsa_kernel _Z11pool_kernelPKfPKiPDF16_
		.amdhsa_group_segment_fixed_size 1024
		.amdhsa_private_segment_fixed_size 0
		.amdhsa_kernarg_size 24
		.amdhsa_user_sgpr_count 2
		.amdhsa_user_sgpr_dispatch_ptr 0
		.amdhsa_user_sgpr_queue_ptr 0
		.amdhsa_user_sgpr_kernarg_segment_ptr 1
		.amdhsa_user_sgpr_dispatch_id 0
		.amdhsa_user_sgpr_kernarg_preload_length 0
		.amdhsa_user_sgpr_kernarg_preload_offset 0
		.amdhsa_user_sgpr_private_segment_size 0
		.amdhsa_uses_dynamic_stack 0
		.amdhsa_enable_private_segment 0
		.amdhsa_system_sgpr_workgroup_id_x 1
		.amdhsa_system_sgpr_workgroup_id_y 0
		.amdhsa_system_sgpr_workgroup_id_z 0
		.amdhsa_system_sgpr_workgroup_info 0
		.amdhsa_system_vgpr_workitem_id 0
		.amdhsa_next_free_vgpr 50
		.amdhsa_next_free_sgpr 28
		.amdhsa_accum_offset 52
		.amdhsa_reserve_vcc 1
		.amdhsa_float_round_mode_32 0
		.amdhsa_float_round_mode_16_64 0
		.amdhsa_float_denorm_mode_32 3
		.amdhsa_float_denorm_mode_16_64 3
		.amdhsa_dx10_clamp 1
		.amdhsa_ieee_mode 1
		.amdhsa_fp16_overflow 0
		.amdhsa_tg_split 0
		.amdhsa_exception_fp_ieee_invalid_op 0
		.amdhsa_exception_fp_denorm_src 0
		.amdhsa_exception_fp_ieee_div_zero 0
		.amdhsa_exception_fp_ieee_overflow 0
		.amdhsa_exception_fp_ieee_underflow 0
		.amdhsa_exception_fp_ieee_inexact 0
		.amdhsa_exception_int_div_zero 0
	.end_amdhsa_kernel

amdhsa.kernels:
  - .agpr_count:     0
    .args:
      - .actual_access:  read_only
        .address_space:  global
        .offset:         0
        .size:           8
        .value_kind:     global_buffer
      - .actual_access:  read_only
        .address_space:  global
        .offset:         8
        .size:           8
        .value_kind:     global_buffer
      - .actual_access:  read_only
        .address_space:  global
        .offset:         16
        .size:           8
        .value_kind:     global_buffer
      - .actual_access:  read_only
        .address_space:  global
        .offset:         24
        .size:           8
        .value_kind:     global_buffer
      - .actual_access:  read_only
        .address_space:  global
        .offset:         32
        .size:           8
        .value_kind:     global_buffer
      - .actual_access:  write_only
        .address_space:  global
        .offset:         40
        .size:           8
        .value_kind:     global_buffer
      - .actual_access:  write_only
        .address_space:  global
        .offset:         48
        .size:           8
        .value_kind:     global_buffer
      - .actual_access:  write_only
        .address_space:  global
        .offset:         56
        .size:           8
        .value_kind:     global_buffer
    .group_segment_fixed_size: 0
    .kernarg_segment_align: 8
    .kernarg_segment_size: 64
    .language:       OpenCL C
    .language_version:
      - 2
      - 0
    .max_flat_workgroup_size: 256
    .name:           _Z11prep_kernelPKfS0_S0_S0_S0_PDv8_DF16_S2_Pi
    .private_segment_fixed_size: 0
    .sgpr_count:     26
    .sgpr_spill_count: 0
    .symbol:         _Z11prep_kernelPKfS0_S0_S0_S0_PDv8_DF16_S2_Pi.kd
    .uniform_work_group_size: 1
    .uses_dynamic_stack: false
    .vgpr_count:     22
    .vgpr_spill_count: 0
    .wavefront_size: 64
  - .agpr_count:     0
    .args:
      - .actual_access:  read_only
        .address_space:  global
        .offset:         0
        .size:           8
        .value_kind:     global_buffer
      - .actual_access:  read_only
        .address_space:  global
        .offset:         8
        .size:           8
        .value_kind:     global_buffer
      - .actual_access:  read_only
        .address_space:  global
        .offset:         16
        .size:           8
        .value_kind:     global_buffer
      - .actual_access:  read_only
        .address_space:  global
        .offset:         24
        .size:           8
        .value_kind:     global_buffer
      - .actual_access:  read_only
        .address_space:  global
        .offset:         32
        .size:           8
        .value_kind:     global_buffer
      - .actual_access:  read_only
        .address_space:  global
        .offset:         40
        .size:           8
        .value_kind:     global_buffer
      - .actual_access:  read_only
        .address_space:  global
        .offset:         48
        .size:           8
        .value_kind:     global_buffer
      - .actual_access:  read_only
        .address_space:  global
        .offset:         56
        .size:           8
        .value_kind:     global_buffer
      - .actual_access:  read_only
        .address_space:  global
        .offset:         64
        .size:           8
        .value_kind:     global_buffer
      - .actual_access:  read_only
        .address_space:  global
        .offset:         72
        .size:           8
        .value_kind:     global_buffer
      - .actual_access:  read_only
        .address_space:  global
        .offset:         80
        .size:           8
        .value_kind:     global_buffer
      - .actual_access:  read_only
        .address_space:  global
        .offset:         88
        .size:           8
        .value_kind:     global_buffer
      - .actual_access:  read_only
        .address_space:  global
        .offset:         96
        .size:           8
        .value_kind:     global_buffer
      - .actual_access:  read_only
        .address_space:  global
        .offset:         104
        .size:           8
        .value_kind:     global_buffer
      - .actual_access:  write_only
        .address_space:  global
        .offset:         112
        .size:           8
        .value_kind:     global_buffer
      - .offset:         120
        .size:           4
        .value_kind:     by_value
      - .actual_access:  read_only
        .address_space:  global
        .offset:         128
        .size:           8
        .value_kind:     global_buffer
      - .actual_access:  read_only
        .address_space:  global
        .offset:         136
        .size:           8
        .value_kind:     global_buffer
      - .actual_access:  write_only
        .address_space:  global
        .offset:         144
        .size:           8
        .value_kind:     global_buffer
      - .actual_access:  read_only
        .address_space:  global
        .offset:         152
        .size:           8
        .value_kind:     global_buffer
      - .actual_access:  read_only
        .address_space:  global
        .offset:         160
        .size:           8
        .value_kind:     global_buffer
      - .address_space:  global
        .offset:         168
        .size:           8
        .value_kind:     global_buffer
      - .actual_access:  write_only
        .address_space:  global
        .offset:         176
        .size:           8
        .value_kind:     global_buffer
      - .address_space:  global
        .offset:         184
        .size:           8
        .value_kind:     global_buffer
      - .actual_access:  write_only
        .address_space:  global
        .offset:         192
        .size:           8
        .value_kind:     global_buffer
      - .actual_access:  write_only
        .address_space:  global
        .offset:         200
        .size:           8
        .value_kind:     global_buffer
    .group_segment_fixed_size: 22528
    .kernarg_segment_align: 8
    .kernarg_segment_size: 208
    .language:       OpenCL C
    .language_version:
      - 2
      - 0
    .max_flat_workgroup_size: 256
    .name:           _Z12embed_kernelPKiS0_S0_S0_S0_PKfS2_S2_S2_S2_S2_S2_S2_PKDv8_DF16_PfiS2_S2_PS3_S0_S0_PiS8_S8_P15HIP_vector_typeIiLj2EES8_
    .private_segment_fixed_size: 0
    .sgpr_count:     44
    .sgpr_spill_count: 0
    .symbol:         _Z12embed_kernelPKiS0_S0_S0_S0_PKfS2_S2_S2_S2_S2_S2_S2_PKDv8_DF16_PfiS2_S2_PS3_S0_S0_PiS8_S8_P15HIP_vector_typeIiLj2EES8_.kd
    .uniform_work_group_size: 1
    .uses_dynamic_stack: false
    .vgpr_count:     166
    .vgpr_spill_count: 0
    .wavefront_size: 64
  - .agpr_count:     0
    .args:
      - .actual_access:  read_only
        .address_space:  global
        .offset:         0
        .size:           8
        .value_kind:     global_buffer
      - .actual_access:  read_only
        .address_space:  global
        .offset:         8
        .size:           8
        .value_kind:     global_buffer
      - .actual_access:  read_only
        .address_space:  global
        .offset:         16
        .size:           8
        .value_kind:     global_buffer
      - .actual_access:  read_only
        .address_space:  global
        .offset:         24
        .size:           8
        .value_kind:     global_buffer
      - .actual_access:  read_only
        .address_space:  global
        .offset:         32
        .size:           8
        .value_kind:     global_buffer
      - .actual_access:  read_only
        .address_space:  global
        .offset:         40
        .size:           8
        .value_kind:     global_buffer
      - .actual_access:  read_only
        .address_space:  global
        .offset:         48
        .size:           8
        .value_kind:     global_buffer
      - .actual_access:  read_only
        .address_space:  global
        .offset:         56
        .size:           8
        .value_kind:     global_buffer
      - .actual_access:  write_only
        .address_space:  global
        .offset:         64
        .size:           8
        .value_kind:     global_buffer
      - .offset:         72
        .size:           4
        .value_kind:     by_value
    .group_segment_fixed_size: 30720
    .kernarg_segment_align: 8
    .kernarg_segment_size: 76
    .language:       OpenCL C
    .language_version:
      - 2
      - 0
    .max_flat_workgroup_size: 256
    .name:           _Z10gru_kernelPKfPKiS2_S2_PK15HIP_vector_typeIiLj2EEPKDv8_DF16_S0_S0_Pfi
    .private_segment_fixed_size: 0
    .sgpr_count:     31
    .sgpr_spill_count: 0
    .symbol:         _Z10gru_kernelPKfPKiS2_S2_PK15HIP_vector_typeIiLj2EEPKDv8_DF16_S0_S0_Pfi.kd
    .uniform_work_group_size: 1
    .uses_dynamic_stack: false
    .vgpr_count:     231
    .vgpr_spill_count: 0
    .wavefront_size: 64
  - .agpr_count:     0
    .args:
      - .actual_access:  read_only
        .address_space:  global
        .offset:         0
        .size:           8
        .value_kind:     global_buffer
      - .actual_access:  read_only
        .address_space:  global
        .offset:         8
        .size:           8
        .value_kind:     global_buffer
      - .actual_access:  write_only
        .address_space:  global
        .offset:         16
        .size:           8
        .value_kind:     global_buffer
    .group_segment_fixed_size: 1024
    .kernarg_segment_align: 8
    .kernarg_segment_size: 24
    .language:       OpenCL C
    .language_version:
      - 2
      - 0
    .max_flat_workgroup_size: 256
    .name:           _Z11pool_kernelPKfPKiPDF16_
    .private_segment_fixed_size: 0
    .sgpr_count:     34
    .sgpr_spill_count: 0
    .symbol:         _Z11pool_kernelPKfPKiPDF16_.kd
    .uniform_work_group_size: 1
    .uses_dynamic_stack: false
    .vgpr_count:     50
    .vgpr_spill_count: 0
    .wavefront_size: 64
  - .agpr_count:     0
    .args:
      - .actual_access:  read_only
        .address_space:  global
        .offset:         0
        .size:           8
        .value_kind:     global_buffer
      - .actual_access:  read_only
        .address_space:  global
        .offset:         8
        .size:           8
        .value_kind:     global_buffer
      - .actual_access:  write_only
        .address_space:  global
        .offset:         16
        .size:           8
        .value_kind:     global_buffer
    .group_segment_fixed_size: 147456
    .kernarg_segment_align: 8
    .kernarg_segment_size: 24
    .language:       OpenCL C
    .language_version:
      - 2
      - 0
    .max_flat_workgroup_size: 256
    .name:           _Z9fc_kernelPKDv8_DF16_S1_Pf
    .private_segment_fixed_size: 0
    .sgpr_count:     17
    .sgpr_spill_count: 0
    .symbol:         _Z9fc_kernelPKDv8_DF16_S1_Pf.kd
    .uniform_work_group_size: 1
    .uses_dynamic_stack: false
    .vgpr_count:     208
    .vgpr_spill_count: 0
    .wavefront_size: 64
